# S5 full-scan loop: the next time block's two global inputs are requested at the top of the current block instead of load-then-wait on the spot (64 blocks per wave)
# baseline (speedup 1.0000x reference)
; #define LAS __attribute__((address_space(3)))
; __device__ __forceinline__ unsigned pk2(float lo, float hi) { const f32x2 v = {lo, hi}; return __builtin_bit_cast(unsigned, __builtin_convertvector(v, nbf16x2)); }
; template <bool FULL>
; __device__ __forceinline__ void s5_task(const In& in, unsigned char* ws, LAS unsigned char* wlds, int b, int g, int ch, int lane) {
;     ...
;     const bf16_t* U = (const bf16_t*)(ws + WS_U);
;     f32x4 dsk = (f32x4){0.f, 0.f, 0.f, 0.f};
;     if (FULL) dsk = *(const f32x4*)(in.ssm_d + g * 16 + 4 * q);
;     const size_t row00 = (size_t)b * SEQ + (size_t)ch * 1024;
;     for (int sb = 0; sb < 64; ++sb) {
;         const size_t row0 = row00 + 16 * sb;
;         bf16x8 ufr = (bf16x8){0, 0, 0, 0, 0, 0, 0, 0};
;         if (q < 2) ufr = *(const bf16x8*)(U + (row0 + col) * 512 + g * 16 + 8 * q);
; #pragma unroll
;         for (int pt = 0; pt < 4; ++pt) {
;             const f32x4 dr = __builtin_amdgcn_mfma_f32_16x16x32_bf16(afr[2 * pt], ufr, (f32x4){0.f, 0.f, 0.f, 0.f}, 0, 0, 0);
;             const f32x4 di = __builtin_amdgcn_mfma_f32_16x16x32_bf16(afr[2 * pt + 1], ufr, (f32x4){0.f, 0.f, 0.f, 0.f}, 0, 0, 0);
;             u32x4 w; w.x = pk2(dr[0], di[0]); w.y = pk2(dr[1], di[1]); w.z = pk2(dr[2], di[2]); w.w = pk2(dr[3], di[3]);
;             *(LAS u32x4*)(BU + col * 68 + 16 * pt + 4 * q) = w; }
;         asm volatile("s_waitcnt lgkmcnt(0)" ::: "memory");
.LBB0_954:
	s_add_i32 s3, s0, 0
	s_ashr_i32 s0, s84, 8
	s_lshl_b32 s1, s1, 6
	s_add_u32 s4, s14, s1
	s_addc_u32 s5, s15, 0
	v_and_b32_e32 v1, 48, v150
	global_load_dwordx4 v[50:53], v1, s[4:5]
	v_and_b32_e32 v70, 15, v0
	s_movk_i32 s8, 0x110
	v_mov_b32_e32 v56, s3
	v_mad_u32_u24 v73, v70, s8, v56
	v_lshrrev_b32_e32 v56, 1, v150
	v_and_b32_e32 v71, 24, v56
	v_lshlrev_b32_e32 v56, 2, v150
	v_add_u32_e32 v72, s3, v56
	v_readlane_b32 s3, v253, 0
	s_ashr_i32 s1, s0, 31
	s_lshl_b32 s3, s3, 14
	s_lshl_b64 s[4:5], s[0:1], 13
	s_lshl_b64 s[0:1], s[0:1], 23
	s_and_b32 s3, s3, 0x700000
	s_or_b32 s0, s0, s3
	v_lshl_or_b32 v56, v70, 10, s0
	s_lshl_b32 s0, s84, 2
	s_and_b32 s3, s0, 0x3e0
	v_or_b32_e32 v56, s3, v56
	v_mov_b32_e32 v57, s1
	v_and_b32_e32 v54, -16, v54
	v_lshl_add_u64 v[54:55], v[56:57], 0, v[54:55]
	s_lshl_b32 s2, s2, 10
	v_lshl_add_u64 v[54:55], s[12:13], 0, v[54:55]
	s_mov_b64 s[0:1], 0x9800000
	v_lshl_add_u64 v[68:69], v[54:55], 0, s[0:1]
	s_or_b32 s0, s4, s2
	v_or_b32_e32 v54, s0, v70
	v_mov_b32_e32 v55, s5
	v_lshlrev_b64 v[54:55], 10, v[54:55]
	v_and_b32_e32 v74, 48, v0
	v_or3_b32 v54, v54, s3, v71
	v_cmp_gt_u32_e64 s[6:7], 32, v150
	v_add_u32_e32 v1, v73, v1
	s_waitcnt vmcnt(1)
	v_mov_b32_e32 v60, v58
	v_mov_b32_e32 v61, v58
	v_mov_b32_e32 v62, v59
	v_mov_b32_e32 v63, v59
	v_pk_mov_b32 v[64:65], v[58:59], v[58:59] op_sel:[1,0]
	v_lshl_add_u64 v[70:71], s[12:13], 0, v[54:55]
	s_mov_b64 s[8:9], 0
	v_add_u32_e32 v73, v73, v74
	s_mov_b32 s0, 0x9800000
	v_add_u32_e32 v74, 0x400, v72
	v_add_u32_e32 v75, 0x800, v72
	v_add_u32_e32 v76, 0xc00, v72
	v_add_co_u32_e32 v106, vcc, s0, v70
	s_nop 1
	v_addc_co_u32_e32 v107, vcc, 0, v71, vcc
	global_load_dwordx2 v[104:105], v[106:107], off
	s_mov_b64 s[2:3], exec
	s_and_b64 exec, exec, s[6:7]
	global_load_dwordx4 v[100:103], v[68:69], off
	s_mov_b64 exec, s[2:3]
	s_branch .LBB0_956
.LBB0_955:
	s_or_b64 exec, exec, s[12:13]
	s_waitcnt vmcnt(0)
	v_mov_b32_e32 v106, v104
	v_mov_b32_e32 v107, v105
	s_add_u32 s2, s8, 0x4000
	s_addc_u32 s3, s9, 0
	s_cmp_eq_u32 s2, 0x100000
	s_cbranch_scc1 .Ls5_nopf
	v_lshl_add_u64 v[108:109], v[68:69], 0, s[2:3]
	s_mov_b64 vcc, exec
	s_and_b64 exec, exec, s[6:7]
	global_load_dwordx4 v[100:103], v[108:109], off
	s_mov_b64 exec, vcc
	v_lshl_add_u64 v[108:109], v[70:71], 0, s[2:3]
	v_add_co_u32_e32 v108, vcc, s0, v108
	s_nop 1
	v_addc_co_u32_e32 v109, vcc, 0, v109, vcc
	global_load_dwordx2 v[104:105], v[108:109], off
.Ls5_nopf:
	v_mfma_f32_16x16x32_bf16 v[78:81], v[10:13], v[54:57], 0
	v_mfma_f32_16x16x32_bf16 v[82:85], v[2:5], v[54:57], 0
	v_mfma_f32_16x16x32_bf16 v[86:89], v[6:9], v[54:57], 0
	v_mfma_f32_16x16x32_bf16 v[90:93], v[14:17], v[54:57], 0
	s_nop 5
	v_cvt_pk_bf16_f32 v78, v78, v82
	v_cvt_pk_bf16_f32 v79, v79, v83
	v_cvt_pk_bf16_f32 v80, v80, v84
	v_cvt_pk_bf16_f32 v81, v81, v85
	ds_write_b128 v1, v[78:81]
	v_cvt_pk_bf16_f32 v78, v86, v90
	v_mfma_f32_16x16x32_bf16 v[82:85], v[18:21], v[54:57], 0
	v_cvt_pk_bf16_f32 v79, v87, v91
	v_cvt_pk_bf16_f32 v80, v88, v92
	v_cvt_pk_bf16_f32 v81, v89, v93
	v_mfma_f32_16x16x32_bf16 v[86:89], v[22:25], v[54:57], 0
	ds_write_b128 v1, v[78:81] offset:64
	v_mfma_f32_16x16x32_bf16 v[90:93], v[26:29], v[54:57], 0
	v_mfma_f32_16x16x32_bf16 v[54:57], v[30:33], v[54:57], 0
	s_nop 4
	v_cvt_pk_bf16_f32 v78, v82, v86
	v_cvt_pk_bf16_f32 v79, v83, v87
	v_cvt_pk_bf16_f32 v80, v84, v88
	v_cvt_pk_bf16_f32 v81, v85, v89
	ds_write_b128 v1, v[78:81] offset:128
	v_cvt_pk_bf16_f32 v54, v90, v54
	v_cvt_pk_bf16_f32 v55, v91, v55
	v_cvt_pk_bf16_f32 v56, v92, v56
	v_cvt_pk_bf16_f32 v57, v93, v57
	ds_write_b128 v1, v[54:57] offset:192
	s_waitcnt lgkmcnt(0)
	ds_read2_b32 v[54:55], v72 offset1:68
	v_pk_mul_f32 v[78:79], v[64:65], v[66:67] op_sel:[0,1]
	s_waitcnt lgkmcnt(0)
	v_lshlrev_b32_e32 v56, 16, v54
	v_pk_fma_f32 v[80:81], v[58:59], v[66:67], v[78:79] neg_lo:[0,0,1] neg_hi:[0,0,1]
	v_pk_fma_f32 v[66:67], v[58:59], v[66:67], v[78:79] op_sel_hi:[1,0,1]
	v_and_b32_e32 v57, 0xffff0000, v54
	v_mov_b32_e32 v81, v67
	v_pk_add_f32 v[56:57], v[80:81], v[56:57]
	v_lshlrev_b32_e32 v54, 16, v55
	v_pk_mul_f32 v[66:67], v[62:63], v[56:57]
	v_cvt_pk_bf16_f32 v77, v56, v57
	v_pk_fma_f32 v[78:79], v[60:61], v[56:57], v[66:67] op_sel:[0,0,1] op_sel_hi:[1,1,0] neg_lo:[0,0,1] neg_hi:[0,0,1]
	v_pk_fma_f32 v[56:57], v[60:61], v[56:57], v[66:67] op_sel:[0,0,1] op_sel_hi:[1,1,0]
	ds_read2_b32 v[66:67], v72 offset0:136 offset1:204
	v_and_b32_e32 v55, 0xffff0000, v55
	v_mov_b32_e32 v79, v57
	v_pk_add_f32 v[54:55], v[78:79], v[54:55]
	s_waitcnt lgkmcnt(0)
	v_and_b32_e32 v57, 0xffff0000, v66
	v_pk_mul_f32 v[78:79], v[62:63], v[54:55]
	v_cvt_pk_bf16_f32 v56, v54, v55
	v_pk_fma_f32 v[80:81], v[60:61], v[54:55], v[78:79] op_sel:[0,0,1] op_sel_hi:[1,1,0] neg_lo:[0,0,1] neg_hi:[0,0,1]
	v_pk_fma_f32 v[54:55], v[60:61], v[54:55], v[78:79] op_sel:[0,0,1] op_sel_hi:[1,1,0]
	ds_write2_b32 v72, v77, v56 offset1:68
	v_lshlrev_b32_e32 v56, 16, v66
	v_mov_b32_e32 v81, v55
	v_pk_add_f32 v[54:55], v[80:81], v[56:57]
	v_lshlrev_b32_e32 v56, 16, v67
	v_and_b32_e32 v57, 0xffff0000, v67
	v_pk_mul_f32 v[66:67], v[62:63], v[54:55]
	v_cvt_pk_bf16_f32 v77, v54, v55
	v_pk_fma_f32 v[78:79], v[60:61], v[54:55], v[66:67] op_sel:[0,0,1] op_sel_hi:[1,1,0] neg_lo:[0,0,1] neg_hi:[0,0,1]
	v_pk_fma_f32 v[54:55], v[60:61], v[54:55], v[66:67] op_sel:[0,0,1] op_sel_hi:[1,1,0]
	ds_read2_b32 v[66:67], v74 offset0:16 offset1:84
	v_mov_b32_e32 v79, v55
	v_pk_add_f32 v[54:55], v[78:79], v[56:57]
	s_waitcnt lgkmcnt(0)
; #define LAS __attribute__((address_space(3)))
; __device__ __forceinline__ unsigned pk2(float lo, float hi) { const f32x2 v = {lo, hi}; return __builtin_bit_cast(unsigned, __builtin_convertvector(v, nbf16x2)); }
; template <bool FULL>
; __device__ __forceinline__ void s5_task(const In& in, unsigned char* ws, LAS unsigned char* wlds, int b, int g, int ch, int lane) {
;     ...
;         for (int t = 0; t < 16; ++t) { const unsigned bw = BU[t * 68 + lane]; const float br = bflo(bw), bi = bfhi(bw);
;             const float nr = ar * xr - ai * xi + br, ni = ar * xi + ai * xr + bi; xr = nr; xi = ni;
;             if (FULL) *(LAS unsigned*)(XB + t * 272 + 4 * lane) = pk2(xr, xi); }
	v_and_b32_e32 v57, 0xffff0000, v66
	v_pk_mul_f32 v[78:79], v[62:63], v[54:55]
	v_cvt_pk_bf16_f32 v56, v54, v55
	v_pk_fma_f32 v[80:81], v[60:61], v[54:55], v[78:79] op_sel:[0,0,1] op_sel_hi:[1,1,0] neg_lo:[0,0,1] neg_hi:[0,0,1]
	v_pk_fma_f32 v[54:55], v[60:61], v[54:55], v[78:79] op_sel:[0,0,1] op_sel_hi:[1,1,0]
	ds_write2_b32 v72, v77, v56 offset0:136 offset1:204
	v_lshlrev_b32_e32 v56, 16, v66
	v_mov_b32_e32 v81, v55
	v_pk_add_f32 v[54:55], v[80:81], v[56:57]
	v_lshlrev_b32_e32 v56, 16, v67
	v_and_b32_e32 v57, 0xffff0000, v67
	v_pk_mul_f32 v[66:67], v[62:63], v[54:55]
	v_cvt_pk_bf16_f32 v77, v54, v55
	v_pk_fma_f32 v[78:79], v[60:61], v[54:55], v[66:67] op_sel:[0,0,1] op_sel_hi:[1,1,0] neg_lo:[0,0,1] neg_hi:[0,0,1]
	v_pk_fma_f32 v[54:55], v[60:61], v[54:55], v[66:67] op_sel:[0,0,1] op_sel_hi:[1,1,0]
	ds_read2_b32 v[66:67], v74 offset0:152 offset1:220
	v_mov_b32_e32 v79, v55
	v_pk_add_f32 v[54:55], v[78:79], v[56:57]
	s_waitcnt lgkmcnt(0)
	v_and_b32_e32 v57, 0xffff0000, v66
	v_pk_mul_f32 v[78:79], v[62:63], v[54:55]
	v_cvt_pk_bf16_f32 v56, v54, v55
	v_pk_fma_f32 v[80:81], v[60:61], v[54:55], v[78:79] op_sel:[0,0,1] op_sel_hi:[1,1,0] neg_lo:[0,0,1] neg_hi:[0,0,1]
	v_pk_fma_f32 v[54:55], v[60:61], v[54:55], v[78:79] op_sel:[0,0,1] op_sel_hi:[1,1,0]
	ds_write2_b32 v74, v77, v56 offset0:16 offset1:84
	v_lshlrev_b32_e32 v56, 16, v66
	v_mov_b32_e32 v81, v55
	v_pk_add_f32 v[54:55], v[80:81], v[56:57]
	v_lshlrev_b32_e32 v56, 16, v67
	v_and_b32_e32 v57, 0xffff0000, v67
	v_pk_mul_f32 v[66:67], v[62:63], v[54:55]
	v_cvt_pk_bf16_f32 v77, v54, v55
	v_pk_fma_f32 v[78:79], v[60:61], v[54:55], v[66:67] op_sel:[0,0,1] op_sel_hi:[1,1,0] neg_lo:[0,0,1] neg_hi:[0,0,1]
	v_pk_fma_f32 v[54:55], v[60:61], v[54:55], v[66:67] op_sel:[0,0,1] op_sel_hi:[1,1,0]
	ds_read2_b32 v[66:67], v75 offset0:32 offset1:100
	v_mov_b32_e32 v79, v55
	v_pk_add_f32 v[54:55], v[78:79], v[56:57]
	s_waitcnt lgkmcnt(0)
	v_and_b32_e32 v57, 0xffff0000, v66
	v_pk_mul_f32 v[78:79], v[62:63], v[54:55]
	v_cvt_pk_bf16_f32 v56, v54, v55
	v_pk_fma_f32 v[80:81], v[60:61], v[54:55], v[78:79] op_sel:[0,0,1] op_sel_hi:[1,1,0] neg_lo:[0,0,1] neg_hi:[0,0,1]
	v_pk_fma_f32 v[54:55], v[60:61], v[54:55], v[78:79] op_sel:[0,0,1] op_sel_hi:[1,1,0]
	ds_write2_b32 v74, v77, v56 offset0:152 offset1:220
	v_lshlrev_b32_e32 v56, 16, v66
	v_mov_b32_e32 v81, v55
	v_pk_add_f32 v[54:55], v[80:81], v[56:57]
	v_lshlrev_b32_e32 v56, 16, v67
	v_and_b32_e32 v57, 0xffff0000, v67
	v_pk_mul_f32 v[66:67], v[62:63], v[54:55]
	v_cvt_pk_bf16_f32 v77, v54, v55
	v_pk_fma_f32 v[78:79], v[60:61], v[54:55], v[66:67] op_sel:[0,0,1] op_sel_hi:[1,1,0] neg_lo:[0,0,1] neg_hi:[0,0,1]
	v_pk_fma_f32 v[54:55], v[60:61], v[54:55], v[66:67] op_sel:[0,0,1] op_sel_hi:[1,1,0]
	ds_read2_b32 v[66:67], v75 offset0:168 offset1:236
	v_mov_b32_e32 v79, v55
	v_pk_add_f32 v[54:55], v[78:79], v[56:57]
	s_waitcnt lgkmcnt(0)
	v_and_b32_e32 v57, 0xffff0000, v66
	v_pk_mul_f32 v[78:79], v[62:63], v[54:55]
	v_cvt_pk_bf16_f32 v56, v54, v55
	v_pk_fma_f32 v[80:81], v[60:61], v[54:55], v[78:79] op_sel:[0,0,1] op_sel_hi:[1,1,0] neg_lo:[0,0,1] neg_hi:[0,0,1]
	v_pk_fma_f32 v[54:55], v[60:61], v[54:55], v[78:79] op_sel:[0,0,1] op_sel_hi:[1,1,0]
	ds_write2_b32 v75, v77, v56 offset0:32 offset1:100
	v_lshlrev_b32_e32 v56, 16, v66
	v_mov_b32_e32 v81, v55
	v_pk_add_f32 v[54:55], v[80:81], v[56:57]
	v_lshlrev_b32_e32 v56, 16, v67
	v_and_b32_e32 v57, 0xffff0000, v67
	v_pk_mul_f32 v[66:67], v[62:63], v[54:55]
	v_cvt_pk_bf16_f32 v77, v54, v55
	v_pk_fma_f32 v[78:79], v[60:61], v[54:55], v[66:67] op_sel:[0,0,1] op_sel_hi:[1,1,0] neg_lo:[0,0,1] neg_hi:[0,0,1]
	v_pk_fma_f32 v[54:55], v[60:61], v[54:55], v[66:67] op_sel:[0,0,1] op_sel_hi:[1,1,0]
	ds_read2_b32 v[66:67], v76 offset0:48 offset1:116
	v_mov_b32_e32 v79, v55
	v_pk_add_f32 v[54:55], v[78:79], v[56:57]
	s_waitcnt lgkmcnt(0)
	v_and_b32_e32 v57, 0xffff0000, v66
	v_pk_mul_f32 v[78:79], v[62:63], v[54:55]
	v_cvt_pk_bf16_f32 v56, v54, v55
	v_pk_fma_f32 v[80:81], v[60:61], v[54:55], v[78:79] op_sel:[0,0,1] op_sel_hi:[1,1,0] neg_lo:[0,0,1] neg_hi:[0,0,1]
	v_pk_fma_f32 v[54:55], v[60:61], v[54:55], v[78:79] op_sel:[0,0,1] op_sel_hi:[1,1,0]
	ds_write2_b32 v75, v77, v56 offset0:168 offset1:236
	v_lshlrev_b32_e32 v56, 16, v66
	v_mov_b32_e32 v81, v55
	v_pk_add_f32 v[54:55], v[80:81], v[56:57]
	v_lshlrev_b32_e32 v56, 16, v67
	v_and_b32_e32 v57, 0xffff0000, v67
	v_pk_mul_f32 v[66:67], v[62:63], v[54:55]
	v_cvt_pk_bf16_f32 v77, v54, v55
	v_pk_fma_f32 v[78:79], v[60:61], v[54:55], v[66:67] op_sel:[0,0,1] op_sel_hi:[1,1,0] neg_lo:[0,0,1] neg_hi:[0,0,1]
	v_pk_fma_f32 v[54:55], v[60:61], v[54:55], v[66:67] op_sel:[0,0,1] op_sel_hi:[1,1,0]
	ds_read2_b32 v[66:67], v76 offset0:184 offset1:252
	v_mov_b32_e32 v79, v55
	v_pk_add_f32 v[54:55], v[78:79], v[56:57]
	s_waitcnt lgkmcnt(0)
; #define LAS __attribute__((address_space(3)))
; __device__ __forceinline__ unsigned pk2(float lo, float hi) { const f32x2 v = {lo, hi}; return __builtin_bit_cast(unsigned, __builtin_convertvector(v, nbf16x2)); }
; __device__ __forceinline__ float gelu_tanh(float x) { const float u = 0.7978845608028654f * (x + 0.044715f * x * x * x); const float e = __expf(2.0f * u); return x * (1.0f - 1.0f / (e + 1.0f)); }
; template <bool FULL>
; __device__ __forceinline__ void s5_task(const In& in, unsigned char* ws, LAS unsigned char* wlds, int b, int g, int ch, int lane) {
;     ...
;         const size_t row0 = row00 + 16 * sb;
;         bf16x8 ufr = (bf16x8){0, 0, 0, 0, 0, 0, 0, 0};
;         if (q < 2) ufr = *(const bf16x8*)(U + (row0 + col) * 512 + g * 16 + 8 * q);
;     ...
;         asm volatile("s_waitcnt lgkmcnt(0)" ::: "memory");
;         if (FULL) {
;             f32x4 y = (f32x4){0.f, 0.f, 0.f, 0.f};
; #pragma unroll
;             for (int s = 0; s < 4; ++s) { const bf16x8 xf = *(const LAS bf16x8*)(XB + col * 272 + (32 * s + 8 * q) * 2); y = __builtin_amdgcn_mfma_f32_16x16x32_bf16(cfr[s], xf, y, 0, 0, 0); }
;             const u32x2 uw = *(const u32x2*)(U + (row0 + col) * 512 + g * 16 + 4 * q);
;             const f32x4 uv = (f32x4){bflo(uw.x), bfhi(uw.x), bflo(uw.y), bfhi(uw.y)};
;             y = y + dsk * uv;
;             u32x2 o; o.x = pk2(gelu_tanh(y[0]), gelu_tanh(y[1])); o.y = pk2(gelu_tanh(y[2]), gelu_tanh(y[3]));
;             *(u32x2*)((bf16_t*)(ws + WS_Z) + (row0 + col) * 512 + g * 16 + 4 * q) = o;
;             asm volatile("s_waitcnt lgkmcnt(0)" ::: "memory");
;         }
	v_and_b32_e32 v57, 0xffff0000, v66
	v_pk_mul_f32 v[78:79], v[62:63], v[54:55]
	v_cvt_pk_bf16_f32 v56, v54, v55
	v_pk_fma_f32 v[80:81], v[60:61], v[54:55], v[78:79] op_sel:[0,0,1] op_sel_hi:[1,1,0] neg_lo:[0,0,1] neg_hi:[0,0,1]
	v_pk_fma_f32 v[54:55], v[60:61], v[54:55], v[78:79] op_sel:[0,0,1] op_sel_hi:[1,1,0]
	ds_write2_b32 v76, v77, v56 offset0:48 offset1:116
	v_lshlrev_b32_e32 v56, 16, v66
	v_mov_b32_e32 v81, v55
	v_pk_add_f32 v[54:55], v[80:81], v[56:57]
	v_lshlrev_b32_e32 v56, 16, v67
	v_and_b32_e32 v57, 0xffff0000, v67
	v_pk_mul_f32 v[66:67], v[62:63], v[54:55]
	v_cvt_pk_bf16_f32 v77, v54, v55
	v_pk_fma_f32 v[78:79], v[60:61], v[54:55], v[66:67] op_sel:[0,0,1] op_sel_hi:[1,1,0] neg_lo:[0,0,1] neg_hi:[0,0,1]
	v_pk_fma_f32 v[54:55], v[60:61], v[54:55], v[66:67] op_sel:[0,0,1] op_sel_hi:[1,1,0]
	s_nop 0
	v_mov_b32_e32 v79, v55
	v_pk_add_f32 v[66:67], v[78:79], v[56:57]
	s_nop 0
	v_cvt_pk_bf16_f32 v54, v66, v67
	ds_write2_b32 v76, v77, v54 offset0:184 offset1:252
	s_waitcnt lgkmcnt(0)
	ds_read_b128 v[54:57], v73
	ds_read_b128 v[78:81], v73 offset:64
	s_waitcnt lgkmcnt(1)
	v_mfma_f32_16x16x32_bf16 v[54:57], v[42:45], v[54:57], 0
	s_waitcnt lgkmcnt(0)
	v_mfma_f32_16x16x32_bf16 v[54:57], v[34:37], v[78:81], v[54:57]
	ds_read_b128 v[78:81], v73 offset:128
	ds_read_b128 v[82:85], v73 offset:192
	s_waitcnt lgkmcnt(1)
	v_mfma_f32_16x16x32_bf16 v[54:57], v[38:41], v[78:81], v[54:57]
	v_lshl_add_u64 v[78:79], v[70:71], 0, s[8:9]
	v_add_co_u32_e32 v80, vcc, s0, v78
	s_waitcnt lgkmcnt(0)
	v_mfma_f32_16x16x32_bf16 v[54:57], v[46:49], v[82:85], v[54:57]
	v_addc_co_u32_e32 v81, vcc, 0, v79, vcc
	v_mov_b32_e32 v80, v106
	s_add_u32 s8, s8, 0x4000
	s_addc_u32 s9, s9, 0
	s_cmp_lg_u32 s8, 0x100000
	v_mov_b32_e32 v81, v107
	v_lshlrev_b32_e32 v82, 16, v80
	v_and_b32_e32 v83, 0xffff0000, v80
	v_pk_fma_f32 v[54:55], v[50:51], v[82:83], v[54:55]
	v_lshlrev_b32_e32 v80, 16, v81
	v_mul_f32_e32 v77, 0x3d372713, v54
	v_mul_f32_e32 v77, v54, v77
	v_fma_f32 v77, v54, v77, v54
	v_mul_f32_e32 v77, 0x3f4c422a, v77
	v_add_f32_e32 v77, v77, v77
	v_mul_f32_e32 v77, 0x3fb8aa3b, v77
	v_exp_f32_e32 v82, v77
	v_mul_f32_e32 v77, 0x3d372713, v55
	v_mul_f32_e32 v77, v55, v77
	v_fma_f32 v77, v55, v77, v55
	v_mul_f32_e32 v77, 0x3f4c422a, v77
	v_add_f32_e32 v77, v77, v77
	v_mul_f32_e32 v77, 0x3fb8aa3b, v77
	v_exp_f32_e32 v83, v77
	v_and_b32_e32 v81, 0xffff0000, v81
	v_pk_fma_f32 v[56:57], v[52:53], v[80:81], v[56:57]
	v_pk_add_f32 v[82:83], v[82:83], 1.0 op_sel_hi:[1,0]
	s_nop 0
	v_div_scale_f32 v77, s[2:3], v83, v83, 1.0
	v_rcp_f32_e32 v84, v77
	s_nop 0
	v_fma_f32 v80, -v77, v84, 1.0
	v_fmac_f32_e32 v84, v80, v84
	v_div_scale_f32 v80, vcc, 1.0, v83, 1.0
	v_mul_f32_e32 v81, v80, v84
	v_fma_f32 v85, -v77, v81, v80
	v_fmac_f32_e32 v81, v85, v84
	v_fma_f32 v77, -v77, v81, v80
	v_div_scale_f32 v80, s[2:3], v82, v82, 1.0
	v_rcp_f32_e32 v86, v80
	v_div_fmas_f32 v77, v77, v84, v81
	v_div_fixup_f32 v81, v77, v83, 1.0
	v_fma_f32 v77, -v80, v86, 1.0
	v_fmac_f32_e32 v86, v77, v86
	v_div_scale_f32 v77, vcc, 1.0, v82, 1.0
	v_mul_f32_e32 v83, v77, v86
	v_fma_f32 v84, -v80, v83, v77
	v_fmac_f32_e32 v83, v84, v86
	v_fma_f32 v77, -v80, v83, v77
	v_mul_f32_e32 v80, 0x3d372713, v56
	v_mul_f32_e32 v80, v56, v80
	v_fma_f32 v80, v56, v80, v56
	v_mul_f32_e32 v80, 0x3f4c422a, v80
	v_add_f32_e32 v80, v80, v80
	v_mul_f32_e32 v80, 0x3fb8aa3b, v80
	v_exp_f32_e32 v84, v80
	v_mul_f32_e32 v80, 0x3d372713, v57
	v_mul_f32_e32 v80, v57, v80
	v_fma_f32 v80, v57, v80, v57
	v_mul_f32_e32 v80, 0x3f4c422a, v80
	v_add_f32_e32 v80, v80, v80
	v_mul_f32_e32 v80, 0x3fb8aa3b, v80
	v_exp_f32_e32 v85, v80
	v_div_fmas_f32 v77, v77, v86, v83
	v_div_fixup_f32 v80, v77, v82, 1.0
	v_pk_add_f32 v[80:81], v[80:81], 1.0 op_sel_hi:[1,0] neg_lo:[1,0] neg_hi:[1,0]
	v_pk_add_f32 v[82:83], v[84:85], 1.0 op_sel_hi:[1,0]
	v_pk_mul_f32 v[54:55], v[54:55], v[80:81]
	v_div_scale_f32 v77, s[2:3], v83, v83, 1.0
	v_rcp_f32_e32 v84, v77
	v_cvt_pk_bf16_f32 v54, v54, v55
	v_fma_f32 v55, -v77, v84, 1.0
	v_fmac_f32_e32 v84, v55, v84
	v_div_scale_f32 v55, vcc, 1.0, v83, 1.0
	v_mul_f32_e32 v80, v55, v84
	v_fma_f32 v81, -v77, v80, v55
	v_fmac_f32_e32 v80, v81, v84
	v_fma_f32 v55, -v77, v80, v55
	v_div_scale_f32 v77, s[2:3], v82, v82, 1.0
	v_rcp_f32_e32 v85, v77
	v_div_fmas_f32 v55, v55, v84, v80
	v_div_fixup_f32 v81, v55, v83, 1.0
	v_fma_f32 v55, -v77, v85, 1.0
	v_fmac_f32_e32 v85, v55, v85
	v_div_scale_f32 v55, vcc, 1.0, v82, 1.0
	v_mul_f32_e32 v80, v55, v85
	v_fma_f32 v83, -v77, v80, v55
	v_fmac_f32_e32 v80, v83, v85
	v_fma_f32 v55, -v77, v80, v55
	v_div_fmas_f32 v55, v55, v85, v80
	v_div_fixup_f32 v80, v55, v82, 1.0
	v_pk_add_f32 v[80:81], v[80:81], 1.0 op_sel_hi:[1,0] neg_lo:[1,0] neg_hi:[1,0]
	s_nop 0
	v_pk_mul_f32 v[56:57], v[56:57], v[80:81]
	s_nop 0
	v_cvt_pk_bf16_f32 v55, v56, v57
	v_add_co_u32_e32 v56, vcc, 0x32400000, v78
	s_nop 1
	v_addc_co_u32_e32 v57, vcc, 0, v79, vcc
	global_store_dwordx2 v[56:57], v[54:55], off
	s_waitcnt lgkmcnt(0)
	s_cbranch_scc0 .LBB0_958
.LBB0_956:
	v_mov_b32_e32 v54, 0
	v_mov_b32_e32 v55, 0
	v_mov_b32_e32 v56, 0
	v_mov_b32_e32 v57, 0
	s_and_saveexec_b64 s[12:13], s[6:7]
	s_cbranch_execz .LBB0_955
	s_waitcnt vmcnt(0)
	v_mov_b32_e32 v54, v100
	v_mov_b32_e32 v55, v101
	v_mov_b32_e32 v56, v102
	v_mov_b32_e32 v57, v103
	s_branch .LBB0_955
